# v070 + attention C-units: query block index rotated by 2 per step inside each sharing group, so every workgroup gets two edge and two middle blocks
# speedup vs baseline: 1.0093x; 1.0052x over previous
; __global__ void __launch_bounds__(NWAVES * 64, 2) mk_fwd(Args args) {
;     ...
;                 for (int bu = bx; bu < 2048; bu += G, ++bu_idx) {
;                     {   const int target = (bu_idx >= ((bx >> 3) % n_bu)) ? cv_mine : 0;
;                         for (; cv_done < target; ++cv_done, cv_it += G, cv_par ^= 1) {
;                             const int lyr = cv_first + cv_it / 1536, r = cv_it % 1536;
;                             if (r < 1024) { const int mi = lyr * 32 + (r >> 5), nb = ((r & 31) + 8 * ((r >> 6) & 3)) & 31;
;                                 q8_cols_item<true, false>(args.in[11] + (size_t)mi * D * 2048, 2048, nb * 64, ws + WS_WGU + (size_t)mi * 2048 * 1024, (float*)(ws + WS_SB) + (size_t)mi * 2048, CAM, cv_par, wave, lane); }
;                             else { const int r2 = r - 1024, mi = lyr * 32 + (r2 >> 4), nb = ((r2 & 15) + 8 * ((r2 >> 6) & 1)) & 15;
;                                 q8_cols_item<false, true>(args.in[13] + (size_t)mi * D * D, D, nb * 64, ws + WS_WDN + (size_t)mi * D * 1024, (float*)(ws + WS_SBD) + (size_t)mi * D, CAM, cv_par, wave, lane); }
;                         }
;                     }
;                     int c_u = lane & 15, g_u = lane >> 4; asm volatile("" : "+v"(c_u), "+v"(g_u));
;                     const int c = c_u, g = g_u;
;                     if (bu < 1024) {
;                         const int b = bu >> 6, h = (bu >> 3) & 7, ib = bu & 7;
.LBB0_241:
	s_mov_b32 s99, s26
	s_cmp_lg_u32 s72, 0x100
	s_cbranch_scc1 .Lremap_done
	s_and_b32 s98, s26, 0xff
	s_lshr_b32 s99, s26, 8
	s_cmp_lt_u32 s99, 4
	s_cbranch_scc0 .Lremap_win
	s_lshr_b32 vcc_lo, s98, 6
	s_lshl_b32 vcc_hi, s99, 1
	s_lshl_b32 s99, s99, 2
	s_add_i32 s99, s99, vcc_lo
	s_lshl_b32 s99, s99, 6
	s_and_b32 vcc_lo, s98, 7
	s_lshl_b32 vcc_lo, vcc_lo, 3
	s_add_i32 s99, s99, vcc_lo
	s_lshr_b32 vcc_lo, s98, 3
	s_add_i32 vcc_lo, vcc_lo, vcc_hi
	s_and_b32 vcc_lo, vcc_lo, 7
	s_add_i32 s99, s99, vcc_lo
	s_branch .Lremap_done
